# as before plus idle workgroups of the top-k phase (both layers) also take trimmed copy items; mixer-phase copy shares trimmed further
# baseline (speedup 1.0000x reference)
.LBB0_1363:
.LBB0_1365:
.LBB0_1366:
.LBB0_1368:
.LBB0_1370:
.LBB0_1372:
.LBB0_1374:
.LBB0_1378:
.LBB0_1380:
.LBB0_1381:
.LBB0_1383:
.LBB0_1385:
.LBB0_1387:
.LBB0_1388:
.LBB0_1390:
.LBB0_1392:
.LBB0_1393:
.LBB0_1394:
.LBB0_1395:
.LBB0_1397:
.LBB0_1401:
.LBB0_1403:
.LBB0_1404:
.LBB0_1406:
.LBB0_1408:
.LBB0_1410:
.LBB0_1411:
.LBB0_1414:
.LBB0_1418:
.LBB0_1420:
.LBB0_1421:
.LBB0_1423:
.LBB0_1425:
.Lmoe_site_A:
	s_nop 1
	v_writelane_b32 v255, s0, 0
	v_writelane_b32 v255, s1, 1
	v_writelane_b32 v255, s2, 2
	v_writelane_b32 v255, s3, 3
	v_writelane_b32 v255, s4, 4
	v_writelane_b32 v255, s5, 5
	v_writelane_b32 v255, s6, 6
	v_writelane_b32 v255, s7, 7
	v_writelane_b32 v255, s8, 8
	v_writelane_b32 v255, s9, 9
	v_writelane_b32 v255, s10, 10
	v_writelane_b32 v255, s11, 11
	v_writelane_b32 v255, s12, 12
	v_writelane_b32 v255, s13, 13
	v_writelane_b32 v255, s14, 14
	v_writelane_b32 v255, s15, 15
	v_writelane_b32 v255, s16, 16
	v_writelane_b32 v255, s17, 17
	v_writelane_b32 v255, s18, 18
	v_writelane_b32 v255, s19, 19
	v_writelane_b32 v255, s20, 20
	v_writelane_b32 v255, s21, 21
	v_writelane_b32 v255, s22, 22
	v_writelane_b32 v255, s23, 23
	v_writelane_b32 v255, s24, 24
	v_writelane_b32 v255, s25, 25
	v_writelane_b32 v255, s26, 26
	v_writelane_b32 v255, s27, 27
	v_writelane_b32 v255, s28, 28
	v_writelane_b32 v255, s29, 29
	v_writelane_b32 v255, s30, 30
	v_writelane_b32 v255, s31, 31
	v_writelane_b32 v255, s32, 32
	v_writelane_b32 v255, s33, 33
	v_writelane_b32 v255, s34, 34
	v_writelane_b32 v255, s35, 35
	s_movk_i32 s0, 0
	s_movk_i32 s2, 16
	s_mov_b32 s4, 0x7800
	s_mov_b32 s5, 0xd600
	s_mov_b32 s34, 0xd600
	s_branch .Lmoe_p4
.Lmoe_site_B:
	s_nop 1
	v_writelane_b32 v255, s0, 0
	v_writelane_b32 v255, s1, 1
	v_writelane_b32 v255, s2, 2
	v_writelane_b32 v255, s3, 3
	v_writelane_b32 v255, s4, 4
	v_writelane_b32 v255, s5, 5
	v_writelane_b32 v255, s6, 6
	v_writelane_b32 v255, s7, 7
	v_writelane_b32 v255, s8, 8
	v_writelane_b32 v255, s9, 9
	v_writelane_b32 v255, s10, 10
	v_writelane_b32 v255, s11, 11
	v_writelane_b32 v255, s12, 12
	v_writelane_b32 v255, s13, 13
	v_writelane_b32 v255, s14, 14
	v_writelane_b32 v255, s15, 15
	v_writelane_b32 v255, s16, 16
	v_writelane_b32 v255, s17, 17
	v_writelane_b32 v255, s18, 18
	v_writelane_b32 v255, s19, 19
	v_writelane_b32 v255, s20, 20
	v_writelane_b32 v255, s21, 21
	v_writelane_b32 v255, s22, 22
	v_writelane_b32 v255, s23, 23
	v_writelane_b32 v255, s24, 24
	v_writelane_b32 v255, s25, 25
	v_writelane_b32 v255, s26, 26
	v_writelane_b32 v255, s27, 27
	v_writelane_b32 v255, s28, 28
	v_writelane_b32 v255, s29, 29
	v_writelane_b32 v255, s30, 30
	v_writelane_b32 v255, s31, 31
	v_writelane_b32 v255, s32, 32
	v_writelane_b32 v255, s33, 33
	v_writelane_b32 v255, s34, 34
	v_writelane_b32 v255, s35, 35
	s_movk_i32 s0, 1
	s_movk_i32 s2, 8
	s_mov_b32 s4, 0x800
	s_mov_b32 s5, 0x5e00
	s_mov_b32 s34, 0x6000
	s_branch .Lmoe_p4

.Lmoe_site_E:
	s_nop 1
	v_writelane_b32 v255, s0, 0
	v_writelane_b32 v255, s1, 1
	v_writelane_b32 v255, s2, 2
	v_writelane_b32 v255, s3, 3
	v_writelane_b32 v255, s4, 4
	v_writelane_b32 v255, s5, 5
	v_writelane_b32 v255, s6, 6
	v_writelane_b32 v255, s7, 7
	v_writelane_b32 v255, s8, 8
	v_writelane_b32 v255, s9, 9
	v_writelane_b32 v255, s10, 10
	v_writelane_b32 v255, s11, 11
	v_writelane_b32 v255, s12, 12
	v_writelane_b32 v255, s13, 13
	v_writelane_b32 v255, s14, 14
	v_writelane_b32 v255, s15, 15
	v_writelane_b32 v255, s16, 16
	v_writelane_b32 v255, s17, 17
	v_writelane_b32 v255, s18, 18
	v_writelane_b32 v255, s19, 19
	v_writelane_b32 v255, s20, 20
	v_writelane_b32 v255, s21, 21
	v_writelane_b32 v255, s22, 22
	v_writelane_b32 v255, s23, 23
	v_writelane_b32 v255, s24, 24
	v_writelane_b32 v255, s25, 25
	v_writelane_b32 v255, s26, 26
	v_writelane_b32 v255, s27, 27
	v_writelane_b32 v255, s28, 28
	v_writelane_b32 v255, s29, 29
	v_writelane_b32 v255, s30, 30
	v_writelane_b32 v255, s31, 31
	v_writelane_b32 v255, s32, 32
	v_writelane_b32 v255, s33, 33
	v_writelane_b32 v255, s34, 34
	v_writelane_b32 v255, s35, 35
	s_movk_i32 s0, 3
	s_movk_i32 s2, 24
	s_mov_b32 s4, 0xfc00
	s_mov_b32 s5, 0x15a00
	s_mov_b32 s34, 0x15a00
	s_branch .Lmoe_p4
.Lmoe_site_T1:
	s_nop 1
	v_writelane_b32 v255, s0, 0
	v_writelane_b32 v255, s1, 1
	v_writelane_b32 v255, s2, 2
	v_writelane_b32 v255, s3, 3
	v_writelane_b32 v255, s4, 4
	v_writelane_b32 v255, s5, 5
	v_writelane_b32 v255, s6, 6
	v_writelane_b32 v255, s7, 7
	v_writelane_b32 v255, s8, 8
	v_writelane_b32 v255, s9, 9
	v_writelane_b32 v255, s10, 10
	v_writelane_b32 v255, s11, 11
	v_writelane_b32 v255, s12, 12
	v_writelane_b32 v255, s13, 13
	v_writelane_b32 v255, s14, 14
	v_writelane_b32 v255, s15, 15
	v_writelane_b32 v255, s16, 16
	v_writelane_b32 v255, s17, 17
	v_writelane_b32 v255, s18, 18
	v_writelane_b32 v255, s19, 19
	v_writelane_b32 v255, s20, 20
	v_writelane_b32 v255, s21, 21
	v_writelane_b32 v255, s22, 22
	v_writelane_b32 v255, s23, 23
	v_writelane_b32 v255, s24, 24
	v_writelane_b32 v255, s25, 25
	v_writelane_b32 v255, s26, 26
	v_writelane_b32 v255, s27, 27
	v_writelane_b32 v255, s28, 28
	v_writelane_b32 v255, s29, 29
	v_writelane_b32 v255, s30, 30
	v_writelane_b32 v255, s31, 31
	v_writelane_b32 v255, s32, 32
	v_writelane_b32 v255, s33, 33
	v_writelane_b32 v255, s34, 34
	v_writelane_b32 v255, s35, 35
	s_movk_i32 s0, 4
	v_readlane_b32 s20, v252, 32
	s_nop 3
	s_cmp_eq_u32 s20, 0
	s_cbranch_scc1 .Lmoe_T1_l1
	s_movk_i32 s2, 32
	s_movk_i32 s26, 1792
	s_mov_b32 s27, 0x1a00
	s_mov_b32 s28, 0x4000
	s_mov_b32 s29, 0x5e00
	s_mov_b32 s32, 0xbc00
	s_mov_b32 s33, 0x11a00
	s_mov_b32 s5, 0x4600
	s_mov_b32 s35, 0x0
	s_branch .Lmoe_tail

.Lmoe_site_T2:
	s_nop 1
	v_writelane_b32 v255, s0, 0
	v_writelane_b32 v255, s1, 1
	v_writelane_b32 v255, s2, 2
	v_writelane_b32 v255, s3, 3
	v_writelane_b32 v255, s4, 4
	v_writelane_b32 v255, s5, 5
	v_writelane_b32 v255, s6, 6
	v_writelane_b32 v255, s7, 7
	v_writelane_b32 v255, s8, 8
	v_writelane_b32 v255, s9, 9
	v_writelane_b32 v255, s10, 10
	v_writelane_b32 v255, s11, 11
	v_writelane_b32 v255, s12, 12
	v_writelane_b32 v255, s13, 13
	v_writelane_b32 v255, s14, 14
	v_writelane_b32 v255, s15, 15
	v_writelane_b32 v255, s16, 16
	v_writelane_b32 v255, s17, 17
	v_writelane_b32 v255, s18, 18
	v_writelane_b32 v255, s19, 19
	v_writelane_b32 v255, s20, 20
	v_writelane_b32 v255, s21, 21
	v_writelane_b32 v255, s22, 22
	v_writelane_b32 v255, s23, 23
	v_writelane_b32 v255, s24, 24
	v_writelane_b32 v255, s25, 25
	v_writelane_b32 v255, s26, 26
	v_writelane_b32 v255, s27, 27
	v_writelane_b32 v255, s28, 28
	v_writelane_b32 v255, s29, 29
	v_writelane_b32 v255, s30, 30
	v_writelane_b32 v255, s31, 31
	v_writelane_b32 v255, s32, 32
	v_writelane_b32 v255, s33, 33
	v_writelane_b32 v255, s34, 34
	v_writelane_b32 v255, s35, 35
	s_movk_i32 s0, 5
	v_readlane_b32 s20, v252, 32
	s_nop 3
	s_cmp_eq_u32 s20, 0
	s_cbranch_scc1 .Lmoe_T2_l1
	s_movk_i32 s2, 128
	s_movk_i32 s26, 1024
	s_mov_b32 s27, 0x1800
	s_mov_b32 s28, 0x3e00
	s_mov_b32 s29, 0x1e000
	s_mov_b32 s32, 0x23e00
	s_mov_b32 s33, 0x29c00
	s_mov_b32 s5, 0x4000
	s_mov_b32 s35, 0x0
	s_branch .Lmoe_tail

.Lmoe_site_T3:
	s_nop 1
	v_writelane_b32 v255, s0, 0
	v_writelane_b32 v255, s1, 1
	v_writelane_b32 v255, s2, 2
	v_writelane_b32 v255, s3, 3
	v_writelane_b32 v255, s4, 4
	v_writelane_b32 v255, s5, 5
	v_writelane_b32 v255, s6, 6
	v_writelane_b32 v255, s7, 7
	v_writelane_b32 v255, s8, 8
	v_writelane_b32 v255, s9, 9
	v_writelane_b32 v255, s10, 10
	v_writelane_b32 v255, s11, 11
	v_writelane_b32 v255, s12, 12
	v_writelane_b32 v255, s13, 13
	v_writelane_b32 v255, s14, 14
	v_writelane_b32 v255, s15, 15
	v_writelane_b32 v255, s16, 16
	v_writelane_b32 v255, s17, 17
	v_writelane_b32 v255, s18, 18
	v_writelane_b32 v255, s19, 19
	v_writelane_b32 v255, s20, 20
	v_writelane_b32 v255, s21, 21
	v_writelane_b32 v255, s22, 22
	v_writelane_b32 v255, s23, 23
	v_writelane_b32 v255, s24, 24
	v_writelane_b32 v255, s25, 25
	v_writelane_b32 v255, s26, 26
	v_writelane_b32 v255, s27, 27
	v_writelane_b32 v255, s28, 28
	v_writelane_b32 v255, s29, 29
	v_writelane_b32 v255, s30, 30
	v_writelane_b32 v255, s31, 31
	v_writelane_b32 v255, s32, 32
	v_writelane_b32 v255, s33, 33
	v_writelane_b32 v255, s34, 34
	v_writelane_b32 v255, s35, 35
	s_movk_i32 s0, 6
	v_readlane_b32 s20, v252, 32
	s_nop 3
	s_cmp_eq_u32 s20, 0
	s_cbranch_scc1 .Lmoe_T3_l1
	s_movk_i32 s2, 128
	s_movk_i32 s26, 1024
	s_mov_b32 s27, 0x1a00
	s_mov_b32 s28, 0x4000
	s_mov_b32 s29, 0x5e00
	s_mov_b32 s32, 0xbc00
	s_mov_b32 s33, 0x11a00
	s_mov_b32 s5, 0x6600
	s_mov_b32 s35, 0x4600
	s_branch .Lmoe_tail
.Lmoe_T3_l1:
	s_movk_i32 s2, 64
	s_movk_i32 s26, 1536
	s_mov_b32 s27, 0x1800
	s_mov_b32 s28, 0x3e00
	s_mov_b32 s29, 0x1e000
	s_mov_b32 s32, 0x23e00
	s_mov_b32 s33, 0x29c00
	s_mov_b32 s5, 0x6400
	s_mov_b32 s35, 0x4000
	s_branch .Lmoe_tail
.Lmoe_tail:
	s_mov_b64 s[30:31], exec
	s_mov_b64 exec, -1
	v_lshrrev_b32_e32 v16, 6, v0
	v_and_b32_e32 v17, 63, v0
	v_readlane_b32 s20, v252, 32
	v_readfirstlane_b32 s1, v16
	v_readlane_b32 s6, v253, 14
	v_readlane_b32 s7, v253, 15
	s_nop 3
	s_cmp_lt_u32 s90, s2
	s_cbranch_scc1 .Lmoe_exit
	s_sub_u32 s21, s90, s2
	s_lshl_b32 s21, s21, 3
	s_add_u32 s4, s21, s1
	s_add_u32 s4, s4, s35
	s_branch .Lmoe_common

.LBB0_2285:
	s_and_saveexec_b64 s[2:3], s[48:49]
	s_xor_b64 s[6:7], exec, s[2:3]
	v_add_u32_e32 v12, s18, v201
	s_or_saveexec_b64 s[6:7], s[6:7]
	v_mov_b32_e32 v4, -1
	s_xor_b64 exec, exec, s[6:7]
	s_cbranch_execz .LBB0_2180
	v_add_u32_e32 v4, s19, v6
	v_ashrrev_i32_e32 v5, 31, v4
	v_lshl_add_u64 v[6:7], v[4:5], 2, s[80:81]
	global_store_dword v[6:7], v12, off
	s_branch .LBB0_2180
.LBB0_2289:
	s_branch .Lmoe_site_T3
.Lmoe_ret_T3:
	s_getreg_b32 s2, hwreg(HW_REG_XCC_ID, 0, 4)
	s_waitcnt vmcnt(0)
	s_barrier
	s_mov_b64 s[0:1], exec
	v_readlane_b32 s6, v253, 4
	v_readlane_b32 s7, v253, 5
	s_and_b64 s[6:7], s[0:1], s[6:7]
	s_mov_b64 exec, s[6:7]
	s_cbranch_execz .LBB0_2341
	v_readlane_b32 s3, v252, 34
	s_waitcnt vmcnt(0) expcnt(0) lgkmcnt(0)
	s_and_b32 s2, s2, 15
	v_mov_b32_e32 v2, s3
	ds_read_b32 v5, v2
	v_readlane_b32 s3, v252, 35
	s_waitcnt lgkmcnt(0)
	v_cmp_ne_u32_e32 vcc, 0, v5
	v_mov_b32_e32 v2, s3
	ds_read_b32 v4, v2
	s_cbranch_vccnz .LBB0_2305
	v_readlane_b32 s8, v253, 0
	v_readlane_b32 s9, v253, 1
	s_load_dwordx2 s[6:7], s[8:9], 0x4
	s_mov_b32 s8, 1
	s_waitcnt lgkmcnt(0)
	s_mul_i32 s3, s6, s95
	s_mul_i32 s3, s3, s7
	s_branch .LBB0_2293
